# attnA loop: rotating SGPR ring offsets, scalar-base K/V DMA, per-unit lane register for ConvW offsets; NA QK reads pipelined
# speedup vs baseline: 1.0568x; 1.0136x over previous
.LBB0_413:
	v_bfe_u32 v3, v9, 1, 3
	v_ashrrev_i32_e32 v7, 4, v9
	v_lshlrev_b32_e32 v6, 7, v8
	v_and_b32_e32 v10, -2, v7
	v_bitop3_b32 v11, v7, v3, -2 bitop3:0x6c
	v_bitop3_b32 v3, v7, v3, 1 bitop3:0x36
	v_lshrrev_b32_e32 v2, 1, v9
	v_lshl_add_u32 v224, v3, 4, v6
	v_add_u32_e32 v3, 4, v10
	v_bitop3_b32 v3, v3, v2, 7 bitop3:0x78
	v_lshl_add_u32 v221, v3, 4, v6
	v_add_u32_e32 v3, 5, v10
	v_bitop3_b32 v2, v3, v2, 7 bitop3:0x78
	v_lshl_add_u32 v222, v2, 4, v6
	v_bfe_u32 v2, v9, 2, 2
	v_lshl_add_u32 v223, v11, 4, v6
	v_lshlrev_b32_e32 v3, 6, v8
	v_bitop3_b32 v6, v7, v2, -2 bitop3:0x6c
	v_bitop3_b32 v2, v7, v2, 1 bitop3:0x36
	v_lshl_add_u32 v220, v2, 4, v3
	s_waitcnt vmcnt(0)
	s_barrier
	v_add_u32_e32 v2, 0, v223
	v_lshl_add_u32 v163, v6, 4, v3
	v_add_u32_e32 v3, 0, v224
	ds_read_b128 v[6:9], v2
	ds_read_b64 v[10:11], v3
	v_mov_b32_e32 v186, v4
	v_mov_b32_e32 v187, v5
	ds_read_b128 v[12:15], v2 offset:4096
	ds_read_b64 v[16:17], v3 offset:4096
	s_waitcnt lgkmcnt(0)
	v_mfma_scale_f32_32x32x64_f8f6f4 v[32:47], v[6:11], v[182:187], 0, v217, v216 op_sel_hi:[0,0,0] cbsz:2 blgp:2
	v_mov_b32_e32 v180, v0
	v_add_u32_e32 v2, 0, v221
	v_add_u32_e32 v3, 0, v222
	ds_read_b128 v[52:55], v2
	ds_read_b64 v[56:57], v3
	v_mov_b32_e32 v181, v1
	ds_read_b128 v[58:61], v2 offset:4096
	ds_read_b64 v[62:63], v3 offset:4096
	s_waitcnt vmcnt(0) lgkmcnt(0)
	v_mfma_scale_f32_32x32x64_f8f6f4 v[32:47], v[52:57], v[176:181], v[32:47], v217, v216 op_sel_hi:[0,0,0] cbsz:2 blgp:2
	s_cmp_lg_u64 s[12:13], 0
	s_cselect_b64 s[54:55], -1, 0
	s_cmp_lt_u32 s0, 2
	s_mov_b32 s0, 0x3f400000
	s_cselect_b64 s[52:53], -1, 0
	s_mov_b32 s8, s9
	v_mfma_scale_f32_32x32x64_f8f6f4 v[16:31], v[12:17], v[182:187], 0, v217, v216 op_sel_hi:[0,0,0] cbsz:2 blgp:2
	s_nop 4
	v_max_f32_e32 v52, v33, v33
	v_max_f32_e32 v53, v32, v32
	v_max_f32_e32 v52, v53, v52
	v_max3_f32 v52, v52, v34, v35
	v_max3_f32 v52, v52, v36, v37
	v_max3_f32 v52, v52, v38, v39
	v_max3_f32 v52, v52, v40, v41
	v_mfma_scale_f32_32x32x64_f8f6f4 v[16:31], v[58:63], v[176:181], v[16:31], v217, v216 op_sel_hi:[0,0,0] cbsz:2 blgp:2
	v_max3_f32 v52, v52, v42, v43
	v_max3_f32 v52, v52, v44, v45
	v_max3_f32 v52, v52, v46, v47
	s_mov_b32 s10, s9
	s_mov_b32 s11, s9
	s_mov_b32 s12, s9
	s_mov_b32 s13, s9
	s_nop 4
	v_max3_f32 v52, v52, v16, v17
	v_max3_f32 v52, v52, v18, v19
	v_max3_f32 v52, v52, v20, v21
	v_max3_f32 v52, v52, v22, v23
	v_max3_f32 v52, v52, v24, v25
	v_max3_f32 v52, v52, v26, v27
	v_max3_f32 v52, v52, v28, v29
	v_max3_f32 v52, v52, v30, v31
	v_mov_b32_e32 v53, v52
	s_nop 1
	v_permlane32_swap_b32_e32 v52, v53
	v_max_f32_e32 v53, v53, v53
	v_max_f32_e32 v52, v52, v52
	v_max_f32_e32 v52, v52, v53
	v_add_f32_e32 v53, 0x7149f2ca, v52
	v_cmp_ge_f32_e32 vcc, s0, v53
	v_max_f32_e32 v52, 0xf149f2ca, v52
	s_cmp_lg_u64 vcc, exec
	v_add_f32_e32 v52, 2.0, v52
	s_cselect_b64 vcc, -1, 0
	v_cndmask_b32_e32 v52, v219, v52, vcc
	v_add_f32_e32 v53, -4.0, v52
	s_lshl_b32 s0, s46, 2
	v_sub_f32_e32 v32, v32, v53
	v_sub_f32_e32 v33, v33, v53
	v_sub_f32_e32 v34, v34, v53
	v_sub_f32_e32 v35, v35, v53
	v_sub_f32_e32 v36, v36, v53
	v_sub_f32_e32 v37, v37, v53
	v_sub_f32_e32 v38, v38, v53
	v_sub_f32_e32 v39, v39, v53
	v_sub_f32_e32 v40, v40, v53
	v_sub_f32_e32 v41, v41, v53
	v_sub_f32_e32 v42, v42, v53
	v_sub_f32_e32 v43, v43, v53
	v_sub_f32_e32 v44, v44, v53
	v_sub_f32_e32 v45, v45, v53
	v_sub_f32_e32 v46, v46, v53
	v_sub_f32_e32 v47, v47, v53
	s_add_i32 s0, s0, 0
	s_mov_b32 s14, s9
	s_mov_b32 s15, s9
	s_mov_b32 s16, s9
	s_mov_b32 s17, s9
	s_mov_b32 s18, s9
	s_mov_b32 s19, s9
	s_mov_b32 s20, s9
	s_mov_b32 s21, s9
	s_mov_b32 s22, s9
	s_mov_b32 s23, s9
	v_mov_b64_e32 v[0:1], s[8:9]
	v_exp_f32_e32 v144, v32
	v_exp_f32_e32 v145, v33
	v_exp_f32_e32 v146, v34
	v_exp_f32_e32 v147, v35
	v_exp_f32_e32 v148, v36
	v_exp_f32_e32 v149, v37
	v_exp_f32_e32 v150, v38
	v_exp_f32_e32 v151, v39
	v_exp_f32_e32 v152, v40
	v_exp_f32_e32 v153, v41
	v_exp_f32_e32 v154, v42
	v_exp_f32_e32 v155, v43
	v_exp_f32_e32 v156, v44
	v_exp_f32_e32 v157, v45
	v_exp_f32_e32 v158, v46
	v_exp_f32_e32 v159, v47
	s_add_i32 s0, s0, 0x1c800
	v_mov_b64_e32 v[2:3], s[10:11]
	v_mov_b64_e32 v[4:5], s[12:13]
	v_mov_b64_e32 v[6:7], s[14:15]
	v_mov_b64_e32 v[8:9], s[16:17]
	v_mov_b64_e32 v[10:11], s[18:19]
	v_mov_b64_e32 v[12:13], s[20:21]
	v_mov_b64_e32 v[14:15], s[22:23]
	v_sub_f32_e32 v128, v16, v53
	s_and_b64 s[10:11], s[52:53], exec
	v_lshlrev_b32_e32 v16, 7, v48
	v_sub_f32_e32 v80, 4.0, v52
	v_sub_f32_e32 v143, v31, v53
	v_sub_f32_e32 v142, v30, v53
	v_sub_f32_e32 v141, v29, v53
	v_sub_f32_e32 v140, v28, v53
	v_sub_f32_e32 v139, v27, v53
	v_sub_f32_e32 v138, v26, v53
	v_sub_f32_e32 v137, v25, v53
	v_sub_f32_e32 v136, v24, v53
	v_sub_f32_e32 v135, v23, v53
	v_sub_f32_e32 v134, v22, v53
	v_sub_f32_e32 v133, v21, v53
	v_sub_f32_e32 v132, v20, v53
	v_sub_f32_e32 v131, v19, v53
	v_sub_f32_e32 v130, v18, v53
	v_sub_f32_e32 v129, v17, v53
	s_cselect_b32 s14, 23, 22
	v_add3_u32 v164, s85, v16, v51
	s_add_u32 s10, s78, s4
	v_add_u32_e32 v174, v49, v50
	v_mov_b64_e32 v[62:63], v[14:15]
	v_mov_b64_e32 v[46:47], v[14:15]
	v_mov_b64_e32 v[30:31], v[14:15]
	v_mov_b64_e32 v[78:79], v[14:15]
	s_mov_b32 s1, 2
	s_mov_b32 s57, 1
	s_mov_b32 s27, -2
	v_mov_b32_e32 v81, v80
	v_mov_b32_e32 v82, v80
	v_mov_b32_e32 v83, v80
	v_mov_b32_e32 v84, v80
	v_mov_b32_e32 v85, v80
	v_mov_b32_e32 v86, v80
	v_mov_b32_e32 v87, v80
	v_mov_b32_e32 v88, v80
	v_mov_b32_e32 v89, v80
	v_mov_b32_e32 v90, v80
	v_mov_b32_e32 v91, v80
	v_mov_b32_e32 v92, v80
	v_mov_b32_e32 v93, v80
	v_mov_b32_e32 v94, v80
	v_mov_b32_e32 v95, v80
	s_mov_b32 s15, 0
	v_mov_b32_e32 v165, v167
	s_addc_u32 s11, s79, s5
	v_mov_b32_e32 v175, v167
	v_mov_b64_e32 v[60:61], v[12:13]
	v_mov_b64_e32 v[58:59], v[10:11]
	v_mov_b64_e32 v[56:57], v[8:9]
	v_mov_b64_e32 v[54:55], v[6:7]
	v_mov_b64_e32 v[52:53], v[4:5]
	v_mov_b64_e32 v[50:51], v[2:3]
	v_mov_b64_e32 v[48:49], v[0:1]
	v_mov_b64_e32 v[44:45], v[12:13]
	v_mov_b64_e32 v[42:43], v[10:11]
	v_mov_b64_e32 v[40:41], v[8:9]
	v_mov_b64_e32 v[38:39], v[6:7]
	v_mov_b64_e32 v[36:37], v[4:5]
	v_mov_b64_e32 v[34:35], v[2:3]
	v_mov_b64_e32 v[32:33], v[0:1]
	v_mov_b64_e32 v[28:29], v[12:13]
	v_mov_b64_e32 v[26:27], v[10:11]
	v_mov_b64_e32 v[24:25], v[8:9]
	v_mov_b64_e32 v[22:23], v[6:7]
	v_mov_b64_e32 v[20:21], v[4:5]
	v_mov_b64_e32 v[18:19], v[2:3]
	v_mov_b64_e32 v[16:17], v[0:1]
	s_mov_b32 s16, 2
	s_mov_b32 s98, 0
	s_mov_b32 s100, 0x2000
	s_mov_b32 s99, 0x4000
	v_mov_b64_e32 v[76:77], v[12:13]
	v_mov_b64_e32 v[74:75], v[10:11]
	v_mov_b64_e32 v[72:73], v[8:9]
	v_mov_b64_e32 v[70:71], v[6:7]
	v_mov_b64_e32 v[68:69], v[4:5]
	v_mov_b64_e32 v[66:67], v[2:3]
	v_mov_b64_e32 v[64:65], v[0:1]
	v_mbcnt_lo_u32_b32 v200, -1, 0
	v_mbcnt_hi_u32_b32 v200, -1, v200
	v_lshrrev_b32_e32 v201, 3, v200
	v_mul_lo_u32 v201, v201, s56
	v_and_b32_e32 v200, 7, v200
	v_lshl_or_b32 v214, v201, 2, v200
	ds_read_b128 v[228:231], v223 offset:8192
	ds_read_b64 v[232:233], v224 offset:8192
	ds_read_b128 v[234:237], v223 offset:12288
	ds_read_b64 v[238:239], v224 offset:12288
	ds_read_b128 v[240:243], v221 offset:8192
	ds_read_b64 v[244:245], v222 offset:8192
	ds_read_b128 v[246:249], v221 offset:12288
	ds_read_b64 v[250:251], v222 offset:12288
	s_mov_b64 s[4:5], -1
	s_and_b64 vcc, exec, s[60:61]
	s_cbranch_vccz .LBB0_415

.LBB0_417:
	s_add_u32 s12, s10, 0x74006000
	s_addc_u32 s13, s11, 0
	s_add_i32 s8, s89, s99
	s_barrier
	s_add_i32 m0, s89, s98
	s_add_u32 s4, s10, 0x74804000
	global_load_lds_dwordx4 v164, s[12:13]
	s_addc_u32 s5, s11, 0
	s_add_i32 m0, s8, 0x6000
	s_andn2_b64 vcc, exec, s[62:63]
	global_load_lds_dwordx4 v174, s[4:5]
	s_cbranch_vccnz .LBB0_419
	s_add_i32 s8, s1, -1
	s_and_b32 s17, s8, 7
	s_lshr_b32 s8, s8, 3
	s_lshl_b64 s[12:13], s[8:9], 24
	s_add_u32 s12, s58, s12
	s_addc_u32 s13, s59, s13
	s_mul_i32 s4, s17, s56
	s_lshl_b32 s4, s4, 5
	s_add_u32 s12, s12, s4
	s_addc_u32 s13, s13, 0
	s_add_i32 s4, s27, 1
	v_add_lshl_u32 v96, v214, s4, 4
	v_and_b32_e32 v96, 0x70, v96
	v_and_or_b32 v96, v214, -8, v96
	s_lshl_b32 s4, s17, 10
	s_add_i32 s4, s66, s4
	s_add_i32 m0, s4, 0xc800
	s_nop 0
	global_load_lds_dwordx4 v96, s[12:13] nt
.LBB0_419:
	v_add_u32_e32 v225, s98, v163
	v_add_u32_e32 v226, s98, v220
	v_mfma_scale_f32_32x32x64_f8f6f4 v[112:127], v[228:233], v[182:187], v[80:95], v217, v216 op_sel_hi:[0,0,0] cbsz:2 blgp:2
	v_exp_f32_e32 v128, v128
	v_exp_f32_e32 v129, v129
	v_exp_f32_e32 v130, v130
	v_exp_f32_e32 v131, v131
	v_mfma_scale_f32_32x32x64_f8f6f4 v[96:111], v[234:239], v[182:187], v[80:95], v217, v216 op_sel_hi:[0,0,0] cbsz:2 blgp:2
	v_exp_f32_e32 v132, v132
	v_exp_f32_e32 v133, v133
	v_exp_f32_e32 v134, v134
	v_exp_f32_e32 v135, v135
	v_mfma_scale_f32_32x32x64_f8f6f4 v[112:127], v[240:245], v[176:181], v[112:127], v217, v216 op_sel_hi:[0,0,0] cbsz:2 blgp:2
	v_exp_f32_e32 v136, v136
	v_exp_f32_e32 v137, v137
	v_exp_f32_e32 v138, v138
	v_exp_f32_e32 v139, v139
	v_mfma_scale_f32_32x32x64_f8f6f4 v[96:111], v[246:251], v[176:181], v[96:111], v217, v216 op_sel_hi:[0,0,0] cbsz:2 blgp:2
	v_add_u32_e32 v200, s99, v223
	v_add_u32_e32 v201, s99, v224
	v_add_u32_e32 v202, s99, v221
	v_add_u32_e32 v203, s99, v222
	ds_read_b128 v[228:231], v200
	ds_read_b64 v[232:233], v201
	ds_read_b128 v[234:237], v200 offset:4096
	ds_read_b64 v[238:239], v201 offset:4096
	ds_read_b128 v[240:243], v202
	ds_read_b64 v[244:245], v203
	ds_read_b128 v[246:249], v202 offset:4096
	ds_read_b64 v[250:251], v203 offset:4096
	ds_read_b128 v[206:209], v225 offset:24576
	ds_read_b64 v[210:211], v226 offset:24576
	ds_read_b128 v[200:203], v225 offset:26624
	ds_read_b64 v[204:205], v226 offset:26624
	ds_read_b128 v[194:197], v225 offset:28672
	ds_read_b64 v[198:199], v226 offset:28672
	ds_read_b128 v[188:191], v225 offset:30720
	ds_read_b64 v[192:193], v226 offset:30720
	v_exp_f32_e32 v140, v140
	v_exp_f32_e32 v141, v141
	v_exp_f32_e32 v142, v142
	v_exp_f32_e32 v143, v143
	s_nop 0
	v_cvt_scalef32_2xpk16_bf6_f32 v[128:133], v[144:159], v[128:143], 1.0
	s_nop 1
	v_mfma_scale_f32_32x32x64_f8f6f4 v[64:79], v[128:133], v[168:173], v[64:79], v218, v218 op_sel_hi:[0,0,0] cbsz:3 blgp:2
	v_max_f32_e32 v225, v113, v113
	v_max_f32_e32 v226, v112, v112
	v_max_f32_e32 v225, v226, v225
	v_max3_f32 v225, v225, v114, v115
	s_waitcnt lgkmcnt(0)
	v_mfma_scale_f32_32x32x64_f8f6f4 v[0:15], v[128:133], v[206:211], v[0:15], v218, v217 op_sel_hi:[0,0,0] cbsz:3 blgp:2
	v_max3_f32 v225, v225, v116, v117
	v_max3_f32 v225, v225, v118, v119
	v_max3_f32 v225, v225, v120, v121
	v_max3_f32 v225, v225, v122, v123
	v_mfma_scale_f32_32x32x64_f8f6f4 v[48:63], v[128:133], v[200:205], v[48:63], v218, v217 op_sel_hi:[0,0,0] cbsz:3 blgp:2
	v_max3_f32 v225, v225, v124, v125
	v_max3_f32 v225, v225, v126, v127
	v_max3_f32 v225, v225, v96, v97
	v_max3_f32 v225, v225, v98, v99
	v_mfma_scale_f32_32x32x64_f8f6f4 v[32:47], v[128:133], v[194:199], v[32:47], v218, v217 op_sel_hi:[0,0,0] cbsz:3 blgp:2
	v_max3_f32 v225, v225, v100, v101
	v_max3_f32 v225, v225, v102, v103
	v_max3_f32 v225, v225, v104, v105
	v_max3_f32 v225, v225, v106, v107
	v_mfma_scale_f32_32x32x64_f8f6f4 v[16:31], v[128:133], v[188:193], v[16:31], v218, v217 op_sel_hi:[0,0,0] cbsz:3 blgp:2
	v_max3_f32 v225, v225, v108, v109
	v_max3_f32 v225, v225, v110, v111
	v_cmp_ge_f32_e32 vcc, s2, v225
	s_cmp_eq_u64 vcc, exec
	s_cbranch_scc0 .LBB0_444
	s_branch .LBB0_424

.LBB0_428:
	s_add_u32 s12, s10, 0x74008000
	s_addc_u32 s13, s11, 0
	s_add_i32 s8, s89, s98
	s_barrier
	s_add_i32 m0, s89, s100
	s_add_u32 s4, s10, 0x74806000
	global_load_lds_dwordx4 v164, s[12:13]
	s_addc_u32 s5, s11, 0
	s_add_i32 m0, s8, 0x6000
	s_and_b64 vcc, exec, s[60:61]
	global_load_lds_dwordx4 v174, s[4:5]
	s_cbranch_vccnz .LBB0_437
	s_and_b32 s17, s1, 7
	s_cmp_eq_u32 s17, 0
	s_cbranch_scc1 .LBB0_431
	s_lshr_b32 s8, s1, 3
	s_cbranch_execz .LBB0_432
	s_branch .LBB0_436

.LBB0_436:
	s_lshl_b64 s[12:13], s[8:9], 24
	s_add_u32 s12, s58, s12
	s_addc_u32 s13, s59, s13
	s_mul_i32 s4, s17, s56
	s_lshl_b32 s4, s4, 5
	s_add_u32 s12, s12, s4
	s_addc_u32 s13, s13, 0
	v_add_lshl_u32 v128, v214, s27, 4
	v_and_b32_e32 v128, 0x70, v128
	v_and_or_b32 v128, v214, -8, v128
	s_lshl_b32 s4, s17, 10
	s_add_i32 s4, s66, s4
	s_add_i32 m0, s4, 0xc800
	s_nop 0
	global_load_lds_dwordx4 v128, s[12:13] nt
.LBB0_437:
	v_add_u32_e32 v212, s100, v163
	v_add_u32_e32 v213, s100, v220
	v_mfma_scale_f32_32x32x64_f8f6f4 v[144:159], v[228:233], v[182:187], v[80:95], v217, v216 op_sel_hi:[0,0,0] cbsz:2 blgp:2
	v_exp_f32_e32 v96, v96
	v_exp_f32_e32 v97, v97
	v_exp_f32_e32 v98, v98
	v_exp_f32_e32 v99, v99
	v_mfma_scale_f32_32x32x64_f8f6f4 v[128:143], v[234:239], v[182:187], v[80:95], v217, v216 op_sel_hi:[0,0,0] cbsz:2 blgp:2
	v_exp_f32_e32 v100, v100
	v_exp_f32_e32 v101, v101
	v_exp_f32_e32 v102, v102
	v_exp_f32_e32 v103, v103
	v_mfma_scale_f32_32x32x64_f8f6f4 v[144:159], v[240:245], v[176:181], v[144:159], v217, v216 op_sel_hi:[0,0,0] cbsz:2 blgp:2
	v_exp_f32_e32 v104, v104
	v_exp_f32_e32 v105, v105
	v_exp_f32_e32 v106, v106
	v_exp_f32_e32 v107, v107
	v_mfma_scale_f32_32x32x64_f8f6f4 v[128:143], v[246:251], v[176:181], v[128:143], v217, v216 op_sel_hi:[0,0,0] cbsz:2 blgp:2
	v_add_u32_e32 v200, s98, v223
	v_add_u32_e32 v201, s98, v224
	v_add_u32_e32 v202, s98, v221
	v_add_u32_e32 v203, s98, v222
	ds_read_b128 v[228:231], v200
	ds_read_b64 v[232:233], v201
	ds_read_b128 v[234:237], v200 offset:4096
	ds_read_b64 v[238:239], v201 offset:4096
	ds_read_b128 v[240:243], v202
	ds_read_b64 v[244:245], v203
	ds_read_b128 v[246:249], v202 offset:4096
	ds_read_b64 v[250:251], v203 offset:4096
	ds_read_b128 v[206:209], v212 offset:24576
	ds_read_b64 v[210:211], v213 offset:24576
	ds_read_b128 v[200:203], v212 offset:26624
	ds_read_b64 v[204:205], v213 offset:26624
	ds_read_b128 v[194:197], v212 offset:28672
	ds_read_b64 v[198:199], v213 offset:28672
	ds_read_b128 v[188:191], v212 offset:30720
	ds_read_b64 v[192:193], v213 offset:30720
	v_exp_f32_e32 v108, v108
	v_exp_f32_e32 v109, v109
	v_exp_f32_e32 v110, v110
	v_exp_f32_e32 v111, v111
	s_nop 0
	v_cvt_scalef32_2xpk16_bf6_f32 v[96:101], v[112:127], v[96:111], 1.0
	s_nop 1
	v_mfma_scale_f32_32x32x64_f8f6f4 v[64:79], v[96:101], v[168:173], v[64:79], v218, v218 op_sel_hi:[0,0,0] cbsz:3 blgp:2
	v_max_f32_e32 v212, v145, v145
	v_max_f32_e32 v213, v144, v144
	v_max_f32_e32 v212, v213, v212
	v_max3_f32 v212, v212, v146, v147
	s_waitcnt lgkmcnt(0)
	v_mfma_scale_f32_32x32x64_f8f6f4 v[0:15], v[96:101], v[206:211], v[0:15], v218, v217 op_sel_hi:[0,0,0] cbsz:3 blgp:2
	v_max3_f32 v212, v212, v148, v149
	v_max3_f32 v212, v212, v150, v151
	v_max3_f32 v212, v212, v152, v153
	v_max3_f32 v212, v212, v154, v155
	v_mfma_scale_f32_32x32x64_f8f6f4 v[48:63], v[96:101], v[200:205], v[48:63], v218, v217 op_sel_hi:[0,0,0] cbsz:3 blgp:2
	v_max3_f32 v212, v212, v156, v157
	v_max3_f32 v212, v212, v158, v159
	v_max3_f32 v212, v212, v128, v129
	v_max3_f32 v212, v212, v130, v131
	v_mfma_scale_f32_32x32x64_f8f6f4 v[32:47], v[96:101], v[194:199], v[32:47], v218, v217 op_sel_hi:[0,0,0] cbsz:3 blgp:2
	v_max3_f32 v212, v212, v132, v133
	v_max3_f32 v212, v212, v134, v135
	v_max3_f32 v212, v212, v136, v137
	v_max3_f32 v212, v212, v138, v139
	v_mfma_scale_f32_32x32x64_f8f6f4 v[16:31], v[96:101], v[188:193], v[16:31], v218, v217 op_sel_hi:[0,0,0] cbsz:3 blgp:2
	v_max3_f32 v212, v212, v140, v141
	v_max3_f32 v212, v212, v142, v143
	v_cmp_ge_f32_e32 vcc, s2, v212
	s_cmp_eq_u64 vcc, exec
	s_cbranch_scc0 .LBB0_445
	s_branch .LBB0_442

.LBB0_442:
	s_mov_b32 s101, s98
	s_mov_b32 s98, s99
	s_mov_b32 s99, s100
	s_mov_b32 s100, s101
	v_exp_f32_e32 v144, v144
	v_exp_f32_e32 v145, v145
	v_exp_f32_e32 v146, v146
	v_exp_f32_e32 v147, v147
	v_exp_f32_e32 v148, v148
	v_exp_f32_e32 v149, v149
	v_exp_f32_e32 v150, v150
	v_exp_f32_e32 v151, v151
	v_exp_f32_e32 v152, v152
	v_exp_f32_e32 v153, v153
	v_exp_f32_e32 v154, v154
	v_exp_f32_e32 v155, v155
	v_exp_f32_e32 v156, v156
	v_exp_f32_e32 v157, v157
	v_exp_f32_e32 v158, v158
	v_exp_f32_e32 v159, v159
	s_add_i32 s8, s1, 2
	s_add_i32 s27, s27, -2
	s_add_u32 s10, s10, 0x4000
	s_addc_u32 s11, s11, 0
	s_add_i32 s1, s1, -1
	s_cmpk_gt_u32 s1, 0xfc
	s_cbranch_scc1 .LBB0_446
	s_mov_b32 s1, s8
	s_mov_b64 s[4:5], -1
	s_and_b64 vcc, exec, s[60:61]
	s_cbranch_vccnz .LBB0_414
	s_branch .LBB0_415

.LBB0_450:
	s_barrier
	s_and_b64 vcc, exec, s[60:61]
	s_cbranch_vccnz .LBB0_452
	v_mbcnt_lo_u32_b32 v98, -1, 0
	v_mbcnt_hi_u32_b32 v98, -1, v98
	s_mov_b32 m0, s88
	v_ashrrev_i32_e32 v96, 3, v98
	v_add_u32_e32 v96, 56, v96
	v_lshl_add_u32 v98, v98, 2, 4
	v_mad_i64_i32 v[96:97], s[10:11], s56, v96, 0
	v_and_b32_e32 v98, 28, v98
	v_lshl_add_u64 v[96:97], v[96:97], 2, s[58:59]
	v_lshlrev_b32_e32 v166, 2, v98
	v_lshl_add_u64 v[96:97], v[96:97], 0, v[166:167]
	s_mov_b64 s[10:11], 0x1f000000
	v_lshl_add_u64 v[96:97], v[96:97], 0, s[10:11]
	global_load_lds_dwordx4 v[96:97], off nt
.LBB0_452:
	v_mov_b32_e32 v164, 1.0
	s_waitcnt lgkmcnt(0)
	v_mfma_scale_f32_32x32x64_f8f6f4 v[96:111], v[228:233], v[182:187], v[80:95], v217, v216 op_sel_hi:[0,0,0] cbsz:2 blgp:2
	v_mfma_scale_f32_32x32x64_f8f6f4 v[80:95], v[234:239], v[182:187], v[80:95], v217, v216 op_sel_hi:[0,0,0] cbsz:2 blgp:2
	v_mfma_scale_f32_32x32x64_f8f6f4 v[96:111], v[240:245], v[176:181], v[96:111], v217, v216 op_sel_hi:[0,0,0] cbsz:2 blgp:2
	v_mfma_scale_f32_32x32x64_f8f6f4 v[80:95], v[246:251], v[176:181], v[80:95], v217, v216 op_sel_hi:[0,0,0] cbsz:2 blgp:2
	s_mov_b32 s1, s98
	s_add_i32 s8, s1, 0
	v_add_u32_e32 v112, s8, v163
	v_add_u32_e32 v113, s8, v220
	ds_read_b128 v[192:195], v112 offset:24576
	ds_read_b64 v[196:197], v113 offset:24576
	ds_read_b128 v[186:189], v112 offset:26624
	ds_read_b64 v[190:191], v113 offset:26624
	ds_read_b128 v[180:183], v112 offset:28672
	ds_read_b64 v[184:185], v113 offset:28672
	ds_read_b128 v[174:177], v112 offset:30720
	ds_read_b64 v[178:179], v113 offset:30720
	v_max_f32_e32 v112, v97, v97
	v_max_f32_e32 v113, v96, v96
	v_max_f32_e32 v112, v113, v112
	v_max3_f32 v112, v112, v98, v99
	v_max3_f32 v112, v112, v100, v101
	v_max3_f32 v112, v112, v102, v103
	v_max3_f32 v112, v112, v104, v105
	v_max3_f32 v112, v112, v106, v107
	v_max3_f32 v112, v112, v108, v109
	v_max3_f32 v112, v112, v110, v111
	v_max3_f32 v112, v112, v80, v81
	v_max3_f32 v112, v112, v82, v83
	v_max3_f32 v112, v112, v84, v85
	v_max3_f32 v112, v112, v86, v87
	v_max3_f32 v112, v112, v88, v89
	v_max3_f32 v112, v112, v90, v91
	v_max3_f32 v112, v112, v92, v93
	v_max3_f32 v112, v112, v94, v95
	v_mov_b32_e32 v113, v112
	s_nop 1
	v_permlane32_swap_b32_e32 v112, v113
	v_max_f32_e32 v113, v113, v113
	v_max_f32_e32 v112, v112, v112
	v_max_f32_e32 v112, v112, v113
	v_cmp_ge_f32_e32 vcc, s2, v112
	s_cmp_eq_u64 vcc, exec
	s_cbranch_scc0 .LBB0_460

.LBB0_457:
	s_mov_b32 s1, s100
	s_add_i32 s1, s1, 0
	v_add_u32_e32 v112, s1, v163
	v_add_u32_e32 v116, s1, v220
	ds_read_b128 v[130:133], v112 offset:24576
	ds_read_b64 v[134:135], v116 offset:24576
	ds_read_b128 v[124:127], v112 offset:26624
	ds_read_b64 v[128:129], v116 offset:26624
	ds_read_b128 v[118:121], v112 offset:28672
	ds_read_b64 v[122:123], v116 offset:28672
	ds_read_b128 v[112:115], v112 offset:30720
	ds_read_b64 v[116:117], v116 offset:30720
	s_and_b64 vcc, exec, s[60:61]
	s_cbranch_vccnz .LBB0_377
	s_waitcnt vmcnt(0)
	v_mbcnt_lo_u32_b32 v145, -1, 0
	v_mbcnt_hi_u32_b32 v145, -1, v145
	s_andn2_b64 vcc, exec, s[54:55]
	v_and_b32_e32 v144, 7, v145
	s_cbranch_vccz .LBB0_375
	v_mov_b32_e32 v138, 0x42800000
	v_mov_b32_e32 v139, 0x42800000
	v_mov_b32_e32 v136, 0x42800000
	v_mov_b32_e32 v137, 0x42800000
	v_mov_b32_e32 v142, 0x42800000
	v_mov_b32_e32 v143, 0x42800000
	v_mov_b32_e32 v140, 0x42800000
	v_mov_b32_e32 v141, 0x42800000
	s_branch .LBB0_376

.LBB0_469:
	v_lshl_add_u64 v[66:67], v[154:155], 0, s[96:97]
	v_add_co_u32_e32 v70, vcc, 0x52002000, v66
	v_lshl_add_u64 v[68:69], v[156:157], 0, s[96:97]
	s_nop 0
	v_addc_co_u32_e32 v71, vcc, 0, v67, vcc
	global_load_dwordx2 v[164:165], v[70:71], off
	v_add_co_u32_e32 v70, vcc, 0x52002000, v68
	s_and_b32 s1, s3, 0x4000
	s_nop 0
	v_addc_co_u32_e32 v71, vcc, 0, v69, vcc
	v_add_co_u32_e32 v66, vcc, 0x4e002000, v66
	global_load_dwordx2 v[162:163], v[70:71], off
	s_nop 0
	v_addc_co_u32_e32 v67, vcc, 0, v67, vcc
	global_load_dwordx2 v[160:161], v[66:67], off
	v_add_co_u32_e32 v66, vcc, 0x4e002000, v68
	s_add_i32 s72, s1, 0
	s_nop 0
	v_addc_co_u32_e32 v67, vcc, 0, v69, vcc
	v_add3_u32 v0, s72, v199, v189
	v_add3_u32 v98, s72, v197, v189
	global_load_dwordx2 v[158:159], v[66:67], off
	s_cmp_lt_u32 s92, s84
	s_cbranch_scc1 .Lna_skip
	s_cmp_ge_u32 s92, s88
	s_cbranch_scc1 .Lna_skip
	v_add_u32_e32 v0, s72, v189
	v_add_u32_e32 v66, v0, v199
	ds_read_b128 v[66:69], v66 offset:32768
	v_add_u32_e32 v70, v0, v199
	ds_read_b128 v[70:73], v70 offset:40960
	v_add_u32_e32 v98, v0, v197
	ds_read_b128 v[98:101], v98 offset:32768
	v_add_u32_e32 v102, v0, v197
	ds_read_b128 v[102:105], v102 offset:40960
	v_add_u32_e32 v106, v0, v195
	ds_read_b128 v[106:109], v106 offset:32768
	v_add_u32_e32 v110, v0, v195
	ds_read_b128 v[110:113], v110 offset:40960
	v_add_u32_e32 v240, v0, v194
	ds_read_b128 v[240:243], v240 offset:32768
	v_add_u32_e32 v244, v0, v194
	ds_read_b128 v[244:247], v244 offset:40960
	v_add_u32_e32 v248, v0, v193
	ds_read_b128 v[248:251], v248 offset:32768
	s_waitcnt lgkmcnt(8)
	v_mfma_f32_32x32x16_bf16 v[82:97], v[66:69], v[114:117], 0
	s_waitcnt lgkmcnt(7)
	v_mfma_f32_32x32x16_bf16 v[66:81], v[70:73], v[114:117], 0
	s_waitcnt lgkmcnt(6)
	v_mfma_f32_32x32x16_bf16 v[82:97], v[98:101], v[118:121], v[82:97]
	v_add_u32_e32 v98, v0, v193
	ds_read_b128 v[98:101], v98 offset:40960
	s_waitcnt lgkmcnt(6)
	v_mfma_f32_32x32x16_bf16 v[66:81], v[102:105], v[118:121], v[66:81]
	v_add_u32_e32 v102, v0, v192
	ds_read_b128 v[102:105], v102 offset:32768
	s_waitcnt lgkmcnt(6)
	v_mfma_f32_32x32x16_bf16 v[82:97], v[106:109], v[122:125], v[82:97]
	v_add_u32_e32 v106, v0, v192
	ds_read_b128 v[106:109], v106 offset:40960
	s_waitcnt lgkmcnt(6)
	v_mfma_f32_32x32x16_bf16 v[66:81], v[110:113], v[122:125], v[66:81]
	v_add_u32_e32 v110, v0, v191
	ds_read_b128 v[110:113], v110 offset:32768
	s_waitcnt lgkmcnt(6)
	v_mfma_f32_32x32x16_bf16 v[82:97], v[240:243], v[126:129], v[82:97]
	v_add_u32_e32 v240, v0, v191
	ds_read_b128 v[240:243], v240 offset:40960
	s_waitcnt lgkmcnt(6)
	v_mfma_f32_32x32x16_bf16 v[66:81], v[244:247], v[126:129], v[66:81]
	v_add_u32_e32 v244, v0, v190
	ds_read_b128 v[244:247], v244 offset:32768
	s_waitcnt lgkmcnt(6)
	v_mfma_f32_32x32x16_bf16 v[82:97], v[248:251], v[130:133], v[82:97]
	v_add_u32_e32 v248, v0, v190
	ds_read_b128 v[248:251], v248 offset:40960
	s_waitcnt lgkmcnt(6)
	v_mfma_f32_32x32x16_bf16 v[66:81], v[98:101], v[130:133], v[66:81]
	s_waitcnt lgkmcnt(5)
	v_mfma_f32_32x32x16_bf16 v[82:97], v[102:105], v[134:137], v[82:97]
	s_waitcnt lgkmcnt(4)
	v_mfma_f32_32x32x16_bf16 v[66:81], v[106:109], v[134:137], v[66:81]
	s_waitcnt lgkmcnt(3)
	v_mfma_f32_32x32x16_bf16 v[82:97], v[110:113], v[138:141], v[82:97]
	s_waitcnt lgkmcnt(2)
	v_mfma_f32_32x32x16_bf16 v[66:81], v[240:243], v[138:141], v[66:81]
	s_waitcnt lgkmcnt(1)
	v_mfma_f32_32x32x16_bf16 v[82:97], v[244:247], v[142:145], v[82:97]
	s_waitcnt lgkmcnt(0)
	v_mfma_f32_32x32x16_bf16 v[66:81], v[248:251], v[142:145], v[66:81]
	s_add_i32 s72, s2, s92
	v_med3_i32 v239, s72, -7, 7
	v_lshlrev_b32_e32 v239, 7, v239
	v_lshl_add_u32 v239, v183, 2, v239
	v_add_u32_e32 v239, 0x10bbc, v239
	ds_read2_b32 v[206:207], v239 offset0:0 offset1:32
	ds_read2_b32 v[208:209], v239 offset0:1 offset1:33
	ds_read2_b32 v[210:211], v239 offset0:2 offset1:34
	ds_read2_b32 v[212:213], v239 offset0:3 offset1:35
	ds_read2_b32 v[214:215], v239 offset0:8 offset1:40
	ds_read2_b32 v[216:217], v239 offset0:9 offset1:41
	ds_read2_b32 v[218:219], v239 offset0:10 offset1:42
	ds_read2_b32 v[220:221], v239 offset0:11 offset1:43
	ds_read2_b32 v[222:223], v239 offset0:16 offset1:48
	ds_read2_b32 v[224:225], v239 offset0:17 offset1:49
	ds_read2_b32 v[226:227], v239 offset0:18 offset1:50
	ds_read2_b32 v[228:229], v239 offset0:19 offset1:51
	ds_read2_b32 v[230:231], v239 offset0:24 offset1:56
	ds_read2_b32 v[232:233], v239 offset0:25 offset1:57
	ds_read2_b32 v[234:235], v239 offset0:26 offset1:58
	s_waitcnt lgkmcnt(14)
	ds_read2_b32 v[236:237], v239 offset0:27 offset1:59
	v_mov_b32_e32 v238, 0xff800000
	s_nop 11
	s_waitcnt lgkmcnt(0)
	v_add_f32_e32 v206, v82, v206
	v_add_f32_e32 v207, v66, v207
	v_cndmask_b32_e64 v82, v238, v206, s[70:71]
	v_cndmask_b32_e64 v0, v238, v207, s[68:69]
	v_add_f32_e32 v208, v83, v208
	v_add_f32_e32 v209, v67, v209
	v_cndmask_b32_e64 v83, v238, v208, s[66:67]
	v_cndmask_b32_e64 v66, v238, v209, s[64:65]
	v_add_f32_e32 v210, v84, v210
	v_add_f32_e32 v211, v68, v211
	v_cndmask_b32_e64 v84, v238, v210, s[62:63]
	v_cndmask_b32_e64 v67, v238, v211, s[60:61]
	v_add_f32_e32 v212, v85, v212
	v_add_f32_e32 v213, v69, v213
	v_cndmask_b32_e64 v85, v238, v212, s[58:59]
	v_cndmask_b32_e64 v68, v238, v213, s[56:57]
	v_add_f32_e32 v214, v86, v214
	v_add_f32_e32 v215, v70, v215
	v_cndmask_b32_e64 v86, v238, v214, s[54:55]
	v_cndmask_b32_e64 v69, v238, v215, s[52:53]
	v_add_f32_e32 v216, v87, v216
	v_add_f32_e32 v217, v71, v217
	v_cndmask_b32_e64 v87, v238, v216, s[50:51]
	v_cndmask_b32_e64 v70, v238, v217, s[48:49]
	v_add_f32_e32 v218, v88, v218
	v_add_f32_e32 v219, v72, v219
	v_cndmask_b32_e64 v88, v238, v218, s[46:47]
	v_cndmask_b32_e64 v71, v238, v219, s[44:45]
	v_add_f32_e32 v220, v89, v220
	v_add_f32_e32 v221, v73, v221
	v_cndmask_b32_e64 v89, v238, v220, s[42:43]
	v_cndmask_b32_e64 v72, v238, v221, s[40:41]
	v_add_f32_e32 v222, v90, v222
	v_add_f32_e32 v223, v74, v223
	v_cndmask_b32_e64 v90, v238, v222, s[38:39]
	v_cndmask_b32_e64 v73, v238, v223, s[36:37]
	v_add_f32_e32 v224, v91, v224
	v_add_f32_e32 v225, v75, v225
	v_cndmask_b32_e64 v91, v238, v224, s[34:35]
	v_cndmask_b32_e64 v74, v238, v225, s[30:31]
	v_add_f32_e32 v226, v92, v226
	v_add_f32_e32 v227, v76, v227
	v_cndmask_b32_e64 v92, v238, v226, s[28:29]
	v_cndmask_b32_e64 v75, v238, v227, s[26:27]
	v_add_f32_e32 v228, v93, v228
	v_add_f32_e32 v229, v77, v229
	v_cndmask_b32_e64 v93, v238, v228, s[24:25]
	v_cndmask_b32_e64 v76, v238, v229, s[22:23]
	v_add_f32_e32 v230, v94, v230
	v_add_f32_e32 v231, v78, v231
	v_cndmask_b32_e64 v94, v238, v230, s[20:21]
	v_cndmask_b32_e64 v77, v238, v231, s[18:19]
	v_add_f32_e32 v232, v95, v232
	v_add_f32_e32 v233, v79, v233
	v_cndmask_b32_e64 v95, v238, v232, s[16:17]
	v_cndmask_b32_e64 v78, v238, v233, s[14:15]
	v_add_f32_e32 v234, v96, v234
	v_add_f32_e32 v235, v80, v235
	v_cndmask_b32_e64 v96, v238, v234, s[12:13]
	v_cndmask_b32_e64 v79, v238, v235, s[10:11]
	v_add_f32_e32 v236, v97, v236
	v_add_f32_e32 v237, v81, v237
	v_cndmask_b32_e64 v97, v238, v236, s[8:9]
	v_cndmask_b32_e64 v80, v238, v237, s[6:7]

	.amdhsa_kernel _Z6mk_fwd4Args
		.amdhsa_group_segment_fixed_size 0
		.amdhsa_private_segment_fixed_size 0
		.amdhsa_kernarg_size 448
		.amdhsa_user_sgpr_count 2
		.amdhsa_user_sgpr_dispatch_ptr 0
		.amdhsa_user_sgpr_queue_ptr 0
		.amdhsa_user_sgpr_kernarg_segment_ptr 1
		.amdhsa_user_sgpr_dispatch_id 0
		.amdhsa_user_sgpr_kernarg_preload_length 0
		.amdhsa_user_sgpr_kernarg_preload_offset 0
		.amdhsa_user_sgpr_private_segment_size 0
		.amdhsa_uses_dynamic_stack 0
		.amdhsa_enable_private_segment 0
		.amdhsa_system_sgpr_workgroup_id_x 1
		.amdhsa_system_sgpr_workgroup_id_y 0
		.amdhsa_system_sgpr_workgroup_id_z 0
		.amdhsa_system_sgpr_workgroup_info 0
		.amdhsa_system_vgpr_workitem_id 0
		.amdhsa_next_free_vgpr 253
		.amdhsa_next_free_sgpr 102
		.amdhsa_accum_offset 256
		.amdhsa_reserve_vcc 1
		.amdhsa_float_round_mode_32 0
		.amdhsa_float_round_mode_16_64 0
		.amdhsa_float_denorm_mode_32 3
		.amdhsa_float_denorm_mode_16_64 3
		.amdhsa_dx10_clamp 1
		.amdhsa_ieee_mode 1
		.amdhsa_fp16_overflow 0
		.amdhsa_tg_split 0
		.amdhsa_exception_fp_ieee_invalid_op 0
		.amdhsa_exception_fp_denorm_src 0
		.amdhsa_exception_fp_ieee_div_zero 0
		.amdhsa_exception_fp_ieee_overflow 0
		.amdhsa_exception_fp_ieee_underflow 0
		.amdhsa_exception_fp_ieee_inexact 0
		.amdhsa_exception_int_div_zero 0
	.end_amdhsa_kernel

amdhsa.kernels:
  - .agpr_count:     0
    .args:
      - .offset:         0
        .size:           192
        .value_kind:     by_value
      - .offset:         192
        .size:           4
        .value_kind:     hidden_block_count_x
      - .offset:         196
        .size:           4
        .value_kind:     hidden_block_count_y
      - .offset:         200
        .size:           4
        .value_kind:     hidden_block_count_z
      - .offset:         204
        .size:           2
        .value_kind:     hidden_group_size_x
      - .offset:         206
        .size:           2
        .value_kind:     hidden_group_size_y
      - .offset:         208
        .size:           2
        .value_kind:     hidden_group_size_z
      - .offset:         210
        .size:           2
        .value_kind:     hidden_remainder_x
      - .offset:         212
        .size:           2
        .value_kind:     hidden_remainder_y
      - .offset:         214
        .size:           2
        .value_kind:     hidden_remainder_z
      - .offset:         232
        .size:           8
        .value_kind:     hidden_global_offset_x
      - .offset:         240
        .size:           8
        .value_kind:     hidden_global_offset_y
      - .offset:         248
        .size:           8
        .value_kind:     hidden_global_offset_z
      - .offset:         256
        .size:           2
        .value_kind:     hidden_grid_dims
      - .offset:         312
        .size:           4
        .value_kind:     hidden_dynamic_lds_size
    .group_segment_fixed_size: 0
    .kernarg_segment_align: 8
    .kernarg_segment_size: 448
    .language:       OpenCL C
    .language_version:
      - 2
      - 0
    .max_flat_workgroup_size: 512
    .name:           _Z6mk_fwd4Args
    .private_segment_fixed_size: 0
    .sgpr_count:     108
    .sgpr_spill_count: 28
    .symbol:         _Z6mk_fwd4Args.kd
    .uniform_work_group_size: 1
    .uses_dynamic_stack: false
    .vgpr_count:     253
    .vgpr_spill_count: 0
    .wavefront_size: 64
